# v33 + P4 epilogue: all four gate-logit loads of a 16-row block (GDF/GNA x bj0/bj1) issued together at the top (one round trip per block)
# baseline (speedup 1.0000x reference)
; #define LAS __attribute__((address_space(3)))
; __device__ __forceinline__ unsigned pk4_fp8(float a, float b, float c, float d) { int w = 0; w = __builtin_amdgcn_cvt_pk_fp8_f32(a, b, w, false); w = __builtin_amdgcn_cvt_pk_fp8_f32(c, d, w, true); return (unsigned)w; }
; #define PG8_SCHED __builtin_amdgcn_sched_barrier(0)
; template <class Epi, class Sched, bool GATHER, bool F8 = false>
; __device__ __forceinline__ void gemm_phase(LAS unsigned char* lds, const int K, const Sched& S, const Epi& E) {
;     ...
;         if constexpr (F8) { asm volatile("s_nop 15\n\ts_nop 15" ::: "memory"); PG8_SCHED; }
;         typename EpiInit<Epi>::Pre pre;
;         if constexpr (EpiInit<Epi>::value) pre = E.preload(has_next ? nxt : cur, wr, wc, fr, fq);
;         E(acc, cur, wr, wc, fr, fq);
;     __device__ __forceinline__ void operator()(f32x4 (&acc)[2][2][4][2], const Unit& u, int wr, int wc, int fr, int fq) const {
;     ...
;                 const size_t ro = (size_t)(u.row0 + ai * 128 + wr * 64 + m * 16 + fr) * DM + col0;
; #pragma unroll
;                 for (int bj = 0; bj < 2; ++bj) {
;                     const u32x4 gd = *(const u32x4*)(GDF + ro + bj * 32);
;                     const float ed[8] = {bf_lo(gd.x), bf_hi(gd.x), bf_lo(gd.y), bf_hi(gd.y), bf_lo(gd.z), bf_hi(gd.z), bf_lo(gd.w), bf_hi(gd.w)};
;                     if (u.tag == 0) {
;                         const u32x4 gn = *(const u32x4*)(GNA + ro + bj * 32);
;                         const float en[8] = {bf_lo(gn.x), bf_hi(gn.x), bf_lo(gn.y), bf_hi(gn.y), bf_lo(gn.z), bf_hi(gn.z), bf_lo(gn.w), bf_hi(gn.w)};
; #pragma unroll
;                         for (int e = 0; e < 8; ++e) {
;                             const float r = (1.0f + __builtin_amdgcn_exp2f(-1.4426950408889634f * ed[e])) * __builtin_amdgcn_rcpf(1.0f + __builtin_amdgcn_exp2f(-1.4426950408889634f * en[e]));
;                             acc[ai][bj][m][e >> 2][e & 3] *= r; }
;                     } else {
;                         float y[8];
; #pragma unroll
;                         for (int e = 0; e < 8; ++e) y[e] = acc[ai][bj][m][e >> 2][e & 3] * sigmoidf_fast(ed[e]) * (PSCALE * WSCALE_INV * OSCALE_INV);
;                         u32x2 w; w.x = pk4_fp8(y[0], y[1], y[2], y[3]); w.y = pk4_fp8(y[4], y[5], y[6], y[7]);
;                         *(LAS u32x2*)(my + fr * 80 + bj * 32 + fq * 8) = w;
;                     }
;                 }
.LBB0_561:
	s_nop 15
	s_nop 15
	v_add_u32_e32 v4, s76, v164
	v_add_u32_e32 v2, s54, v167
	v_ashrrev_i32_e32 v5, 31, v4
	v_ashrrev_i32_e32 v3, 31, v2
	v_lshlrev_b64 v[6:7], 11, v[4:5]
	v_lshl_add_u64 v[8:9], v[6:7], 0, v[2:3]
	v_lshl_add_u64 v[6:7], v[8:9], 1, s[40:41]
	global_load_dwordx4 v[156:159], v[6:7], off nt
	global_load_dwordx4 v[240:243], v[6:7], off offset:64 nt
	v_lshl_add_u64 v[252:253], v[8:9], 1, s[38:39]
	global_load_dwordx4 v[244:247], v[252:253], off nt
	global_load_dwordx4 v[248:251], v[252:253], off offset:64 nt
	v_cndmask_b32_e64 v5, 0, 1, s[58:59]
	v_cmp_ne_u32_e64 s[4:5], 1, v5
	s_andn2_b64 vcc, exec, s[58:59]
	s_mov_b64 s[58:59], -1
	s_waitcnt vmcnt(0)
	v_lshlrev_b32_e32 v160, 16, v156
	v_and_b32_e32 v156, 0xffff0000, v156
	v_lshlrev_b32_e32 v161, 16, v157
	v_and_b32_e32 v157, 0xffff0000, v157
	v_lshlrev_b32_e32 v162, 16, v158
	v_and_b32_e32 v158, 0xffff0000, v158
	v_lshlrev_b32_e32 v163, 16, v159
	v_and_b32_e32 v159, 0xffff0000, v159
	v_mul_f32_e32 v160, 0xbfb8aa3b, v160
	v_mul_f32_e32 v156, 0xbfb8aa3b, v156
	v_mul_f32_e32 v181, 0xbfb8aa3b, v161
	v_mul_f32_e32 v157, 0xbfb8aa3b, v157
	v_mul_f32_e32 v182, 0xbfb8aa3b, v162
	v_mul_f32_e32 v158, 0xbfb8aa3b, v158
	v_mul_f32_e32 v183, 0xbfb8aa3b, v163
	v_mul_f32_e32 v159, 0xbfb8aa3b, v159
	v_exp_f32_e32 v160, v160
	v_exp_f32_e32 v161, v156
	v_exp_f32_e32 v162, v181
	v_exp_f32_e32 v163, v157
	v_exp_f32_e32 v156, v182
	v_exp_f32_e32 v157, v158
	v_exp_f32_e32 v158, v183
	v_exp_f32_e32 v159, v159
	s_cbranch_vccnz .LBB0_563
	v_add_f32_e32 v182, 1.0, v162
	v_rcp_f32_e32 v182, v182
	v_add_f32_e32 v183, 1.0, v163
	v_rcp_f32_e32 v183, v183
	v_add_f32_e32 v184, 1.0, v156
	v_rcp_f32_e32 v184, v184
	v_mul_f32_e32 v182, v136, v182
	v_mul_f32_e32 v185, 0x3c000000, v182
	v_mul_f32_e32 v182, v137, v183
	v_add_f32_e32 v183, 1.0, v157
	v_mul_f32_e32 v186, 0x3c000000, v182
	v_mul_f32_e32 v182, v130, v184
	v_rcp_f32_e32 v183, v183
	v_add_f32_e32 v184, 1.0, v158
	v_rcp_f32_e32 v184, v184
	v_add_f32_e32 v5, 1.0, v160
	v_add_f32_e32 v181, 1.0, v161
	v_rcp_f32_e32 v5, v5
	v_rcp_f32_e32 v181, v181
	v_mul_f32_e32 v187, 0x3c000000, v182
	v_mul_f32_e32 v182, v131, v183
	v_mul_f32_e32 v188, 0x3c000000, v182
	v_mul_f32_e32 v182, v132, v184
	v_mul_f32_e32 v184, 0x3c000000, v182
	v_add_f32_e32 v182, 1.0, v159
	v_mul_f32_e32 v5, v134, v5
	v_mul_f32_e32 v181, v135, v181
	v_rcp_f32_e32 v189, v182
	v_mul_f32_e32 v5, 0x3c000000, v5
	v_mul_f32_e32 v181, 0x3c000000, v181
	v_mov_b32_e32 v182, 0
	v_mov_b32_e32 v183, 0
	v_cvt_pk_fp8_f32 v182, v5, v181
	v_cvt_pk_fp8_f32 v183, v187, v188
	v_mul_f32_e32 v5, v133, v189
	v_mul_f32_e32 v5, 0x3c000000, v5
	v_cvt_pk_fp8_f32 v182, v185, v186 op_sel:[0,0,1]
	v_cvt_pk_fp8_f32 v183, v184, v5 op_sel:[0,0,1]
	s_mov_b64 s[58:59], 0
	ds_write_b64 v180, v[182:183]

; #define LAS __attribute__((address_space(3)))
; __device__ __forceinline__ unsigned pk4_fp8(float a, float b, float c, float d) { int w = 0; w = __builtin_amdgcn_cvt_pk_fp8_f32(a, b, w, false); w = __builtin_amdgcn_cvt_pk_fp8_f32(c, d, w, true); return (unsigned)w; }
; __device__ __forceinline__ float bf_lo(unsigned w) { return __uint_as_float(w << 16); }
; __device__ __forceinline__ float bf_hi(unsigned w) { return __uint_as_float(w & 0xffff0000u); }
; __device__ __forceinline__ float sigmoidf_fast(float x) { return __builtin_amdgcn_rcpf(1.0f + __builtin_amdgcn_exp2f(-1.4426950408889634f * x)); }
;     __device__ __forceinline__ void operator()(f32x4 (&acc)[2][2][4][2], const Unit& u, int wr, int wc, int fr, int fq) const {
;     ...
;                 const size_t ro = (size_t)(u.row0 + ai * 128 + wr * 64 + m * 16 + fr) * DM + col0;
; #pragma unroll
;                 for (int bj = 0; bj < 2; ++bj) {
;                     const u32x4 gd = *(const u32x4*)(GDF + ro + bj * 32);
;                     const float ed[8] = {bf_lo(gd.x), bf_hi(gd.x), bf_lo(gd.y), bf_hi(gd.y), bf_lo(gd.z), bf_hi(gd.z), bf_lo(gd.w), bf_hi(gd.w)};
;                     if (u.tag == 0) {
;                         const u32x4 gn = *(const u32x4*)(GNA + ro + bj * 32);
;                         const float en[8] = {bf_lo(gn.x), bf_hi(gn.x), bf_lo(gn.y), bf_hi(gn.y), bf_lo(gn.z), bf_hi(gn.z), bf_lo(gn.w), bf_hi(gn.w)};
; #pragma unroll
;                         for (int e = 0; e < 8; ++e) {
;                             const float r = (1.0f + __builtin_amdgcn_exp2f(-1.4426950408889634f * ed[e])) * __builtin_amdgcn_rcpf(1.0f + __builtin_amdgcn_exp2f(-1.4426950408889634f * en[e]));
;                             acc[ai][bj][m][e >> 2][e & 3] *= r; }
;                     } else {
;                         float y[8];
; #pragma unroll
;                         for (int e = 0; e < 8; ++e) y[e] = acc[ai][bj][m][e >> 2][e & 3] * sigmoidf_fast(ed[e]) * (PSCALE * WSCALE_INV * OSCALE_INV);
;                         u32x2 w; w.x = pk4_fp8(y[0], y[1], y[2], y[3]); w.y = pk4_fp8(y[4], y[5], y[6], y[7]);
;                         *(LAS u32x2*)(my + fr * 80 + bj * 32 + fq * 8) = w;
;                     }
;                 }
.LBB0_569:
	s_nop 1
	v_add_u32_e32 v6, s76, v168
	v_ashrrev_i32_e32 v7, 31, v6
	v_lshlrev_b64 v[6:7], 11, v[6:7]
	v_lshl_add_u64 v[6:7], v[6:7], 0, v[2:3]
	v_lshl_add_u64 v[8:9], v[6:7], 1, s[40:41]
	global_load_dwordx4 v[156:159], v[8:9], off nt
	global_load_dwordx4 v[240:243], v[8:9], off offset:64 nt
	v_lshl_add_u64 v[252:253], v[6:7], 1, s[38:39]
	global_load_dwordx4 v[244:247], v[252:253], off nt
	global_load_dwordx4 v[248:251], v[252:253], off offset:64 nt
	s_and_b64 vcc, exec, s[4:5]
	s_mov_b64 s[58:59], -1
	s_waitcnt vmcnt(0)
	v_lshlrev_b32_e32 v5, 16, v156
	v_and_b32_e32 v156, 0xffff0000, v156
	v_lshlrev_b32_e32 v160, 16, v157
	v_and_b32_e32 v157, 0xffff0000, v157
	v_lshlrev_b32_e32 v161, 16, v158
	v_and_b32_e32 v158, 0xffff0000, v158
	v_lshlrev_b32_e32 v162, 16, v159
	v_and_b32_e32 v159, 0xffff0000, v159
	v_mul_f32_e32 v5, 0xbfb8aa3b, v5
	v_mul_f32_e32 v156, 0xbfb8aa3b, v156
	v_mul_f32_e32 v163, 0xbfb8aa3b, v160
	v_mul_f32_e32 v157, 0xbfb8aa3b, v157
	v_mul_f32_e32 v181, 0xbfb8aa3b, v161
	v_mul_f32_e32 v158, 0xbfb8aa3b, v158
	v_mul_f32_e32 v182, 0xbfb8aa3b, v162
	v_mul_f32_e32 v159, 0xbfb8aa3b, v159
	v_exp_f32_e32 v160, v5
	v_exp_f32_e32 v161, v156
	v_exp_f32_e32 v162, v163
	v_exp_f32_e32 v163, v157
	v_exp_f32_e32 v156, v181
	v_exp_f32_e32 v157, v158
	v_exp_f32_e32 v158, v182
	v_exp_f32_e32 v159, v159
	s_cbranch_vccnz .LBB0_571
	v_add_f32_e32 v182, 1.0, v162
	v_rcp_f32_e32 v182, v182
	v_add_f32_e32 v183, 1.0, v163
	v_rcp_f32_e32 v183, v183
	v_add_f32_e32 v184, 1.0, v156
	v_rcp_f32_e32 v184, v184
	v_mul_f32_e32 v182, v128, v182
	v_mul_f32_e32 v185, 0x3c000000, v182
	v_mul_f32_e32 v182, v129, v183
	v_add_f32_e32 v183, 1.0, v157
	v_mul_f32_e32 v186, 0x3c000000, v182
	v_mul_f32_e32 v182, v122, v184
	v_rcp_f32_e32 v183, v183
	v_add_f32_e32 v184, 1.0, v158
	v_rcp_f32_e32 v184, v184
	v_add_f32_e32 v5, 1.0, v160
	v_add_f32_e32 v181, 1.0, v161
	v_rcp_f32_e32 v5, v5
	v_rcp_f32_e32 v181, v181
	v_mul_f32_e32 v187, 0x3c000000, v182
	v_mul_f32_e32 v182, v123, v183
	v_mul_f32_e32 v188, 0x3c000000, v182
	v_mul_f32_e32 v182, v124, v184
	v_mul_f32_e32 v184, 0x3c000000, v182
	v_add_f32_e32 v182, 1.0, v159
	v_mul_f32_e32 v5, v126, v5
	v_mul_f32_e32 v181, v127, v181
	v_rcp_f32_e32 v189, v182
	v_mul_f32_e32 v5, 0x3c000000, v5
	v_mul_f32_e32 v181, 0x3c000000, v181
	v_mov_b32_e32 v182, 0
	v_mov_b32_e32 v183, 0
	v_cvt_pk_fp8_f32 v182, v5, v181
	v_cvt_pk_fp8_f32 v183, v187, v188
	v_mul_f32_e32 v5, v125, v189
	v_mul_f32_e32 v5, 0x3c000000, v5
	v_cvt_pk_fp8_f32 v182, v185, v186 op_sel:[0,0,1]
	v_cvt_pk_fp8_f32 v183, v184, v5 op_sel:[0,0,1]
	s_mov_b64 s[58:59], 0
	ds_write_b64 v180, v[182:183]

; #define LAS __attribute__((address_space(3)))
; __device__ __forceinline__ unsigned pk4_fp8(float a, float b, float c, float d) { int w = 0; w = __builtin_amdgcn_cvt_pk_fp8_f32(a, b, w, false); w = __builtin_amdgcn_cvt_pk_fp8_f32(c, d, w, true); return (unsigned)w; }
; __device__ __forceinline__ float bf_lo(unsigned w) { return __uint_as_float(w << 16); }
; __device__ __forceinline__ float bf_hi(unsigned w) { return __uint_as_float(w & 0xffff0000u); }
; __device__ __forceinline__ float sigmoidf_fast(float x) { return __builtin_amdgcn_rcpf(1.0f + __builtin_amdgcn_exp2f(-1.4426950408889634f * x)); }
;     __device__ __forceinline__ void operator()(f32x4 (&acc)[2][2][4][2], const Unit& u, int wr, int wc, int fr, int fq) const {
;     ...
;                 const size_t ro = (size_t)(u.row0 + ai * 128 + wr * 64 + m * 16 + fr) * DM + col0;
; #pragma unroll
;                 for (int bj = 0; bj < 2; ++bj) {
;                     const u32x4 gd = *(const u32x4*)(GDF + ro + bj * 32);
;                     const float ed[8] = {bf_lo(gd.x), bf_hi(gd.x), bf_lo(gd.y), bf_hi(gd.y), bf_lo(gd.z), bf_hi(gd.z), bf_lo(gd.w), bf_hi(gd.w)};
;                     if (u.tag == 0) {
;                         const u32x4 gn = *(const u32x4*)(GNA + ro + bj * 32);
;                         const float en[8] = {bf_lo(gn.x), bf_hi(gn.x), bf_lo(gn.y), bf_hi(gn.y), bf_lo(gn.z), bf_hi(gn.z), bf_lo(gn.w), bf_hi(gn.w)};
; #pragma unroll
;                         for (int e = 0; e < 8; ++e) {
;                             const float r = (1.0f + __builtin_amdgcn_exp2f(-1.4426950408889634f * ed[e])) * __builtin_amdgcn_rcpf(1.0f + __builtin_amdgcn_exp2f(-1.4426950408889634f * en[e]));
;                             acc[ai][bj][m][e >> 2][e & 3] *= r; }
;                     } else {
;                         float y[8];
; #pragma unroll
;                         for (int e = 0; e < 8; ++e) y[e] = acc[ai][bj][m][e >> 2][e & 3] * sigmoidf_fast(ed[e]) * (PSCALE * WSCALE_INV * OSCALE_INV);
;                         u32x2 w; w.x = pk4_fp8(y[0], y[1], y[2], y[3]); w.y = pk4_fp8(y[4], y[5], y[6], y[7]);
;                         *(LAS u32x2*)(my + fr * 80 + bj * 32 + fq * 8) = w;
;                     }
;                 }
.LBB0_577:
	s_nop 1
	v_add_u32_e32 v6, s76, v171
	v_ashrrev_i32_e32 v7, 31, v6
	v_lshlrev_b64 v[6:7], 11, v[6:7]
	v_lshl_add_u64 v[6:7], v[6:7], 0, v[2:3]
	v_lshl_add_u64 v[8:9], v[6:7], 1, s[40:41]
	global_load_dwordx4 v[156:159], v[8:9], off nt
	global_load_dwordx4 v[240:243], v[8:9], off offset:64 nt
	v_lshl_add_u64 v[252:253], v[6:7], 1, s[38:39]
	global_load_dwordx4 v[244:247], v[252:253], off nt
	global_load_dwordx4 v[248:251], v[252:253], off offset:64 nt
	s_and_b64 vcc, exec, s[4:5]
	s_mov_b64 s[58:59], -1
	s_waitcnt vmcnt(0)
	v_lshlrev_b32_e32 v5, 16, v156
	v_and_b32_e32 v156, 0xffff0000, v156
	v_lshlrev_b32_e32 v160, 16, v157
	v_and_b32_e32 v157, 0xffff0000, v157
	v_lshlrev_b32_e32 v161, 16, v158
	v_and_b32_e32 v158, 0xffff0000, v158
	v_lshlrev_b32_e32 v162, 16, v159
	v_and_b32_e32 v159, 0xffff0000, v159
	v_mul_f32_e32 v5, 0xbfb8aa3b, v5
	v_mul_f32_e32 v156, 0xbfb8aa3b, v156
	v_mul_f32_e32 v163, 0xbfb8aa3b, v160
	v_mul_f32_e32 v157, 0xbfb8aa3b, v157
	v_mul_f32_e32 v181, 0xbfb8aa3b, v161
	v_mul_f32_e32 v158, 0xbfb8aa3b, v158
	v_mul_f32_e32 v182, 0xbfb8aa3b, v162
	v_mul_f32_e32 v159, 0xbfb8aa3b, v159
	v_exp_f32_e32 v160, v5
	v_exp_f32_e32 v161, v156
	v_exp_f32_e32 v162, v163
	v_exp_f32_e32 v163, v157
	v_exp_f32_e32 v156, v181
	v_exp_f32_e32 v157, v158
	v_exp_f32_e32 v158, v182
	v_exp_f32_e32 v159, v159
	s_cbranch_vccnz .LBB0_579
	v_add_f32_e32 v182, 1.0, v162
	v_rcp_f32_e32 v182, v182
	v_add_f32_e32 v183, 1.0, v163
	v_rcp_f32_e32 v183, v183
	v_add_f32_e32 v184, 1.0, v156
	v_rcp_f32_e32 v184, v184
	v_mul_f32_e32 v182, v120, v182
	v_mul_f32_e32 v185, 0x3c000000, v182
	v_mul_f32_e32 v182, v121, v183
	v_add_f32_e32 v183, 1.0, v157
	v_mul_f32_e32 v186, 0x3c000000, v182
	v_mul_f32_e32 v182, v114, v184
	v_rcp_f32_e32 v183, v183
	v_add_f32_e32 v184, 1.0, v158
	v_rcp_f32_e32 v184, v184
	v_add_f32_e32 v5, 1.0, v160
	v_add_f32_e32 v181, 1.0, v161
	v_rcp_f32_e32 v5, v5
	v_rcp_f32_e32 v181, v181
	v_mul_f32_e32 v187, 0x3c000000, v182
	v_mul_f32_e32 v182, v115, v183
	v_mul_f32_e32 v188, 0x3c000000, v182
	v_mul_f32_e32 v182, v116, v184
	v_mul_f32_e32 v184, 0x3c000000, v182
	v_add_f32_e32 v182, 1.0, v159
	v_mul_f32_e32 v5, v118, v5
	v_mul_f32_e32 v181, v119, v181
	v_rcp_f32_e32 v189, v182
	v_mul_f32_e32 v5, 0x3c000000, v5
	v_mul_f32_e32 v181, 0x3c000000, v181
	v_mov_b32_e32 v182, 0
	v_mov_b32_e32 v183, 0
	v_cvt_pk_fp8_f32 v182, v5, v181
	v_cvt_pk_fp8_f32 v183, v187, v188
	v_mul_f32_e32 v5, v117, v189
	v_mul_f32_e32 v5, 0x3c000000, v5
	v_cvt_pk_fp8_f32 v182, v185, v186 op_sel:[0,0,1]
	v_cvt_pk_fp8_f32 v183, v184, v5 op_sel:[0,0,1]
	s_mov_b64 s[58:59], 0
	ds_write_b64 v180, v[182:183]

; #define LAS __attribute__((address_space(3)))
; __device__ __forceinline__ unsigned pk4_fp8(float a, float b, float c, float d) { int w = 0; w = __builtin_amdgcn_cvt_pk_fp8_f32(a, b, w, false); w = __builtin_amdgcn_cvt_pk_fp8_f32(c, d, w, true); return (unsigned)w; }
; __device__ __forceinline__ float bf_lo(unsigned w) { return __uint_as_float(w << 16); }
; __device__ __forceinline__ float bf_hi(unsigned w) { return __uint_as_float(w & 0xffff0000u); }
; __device__ __forceinline__ float sigmoidf_fast(float x) { return __builtin_amdgcn_rcpf(1.0f + __builtin_amdgcn_exp2f(-1.4426950408889634f * x)); }
;     __device__ __forceinline__ void operator()(f32x4 (&acc)[2][2][4][2], const Unit& u, int wr, int wc, int fr, int fq) const {
;     ...
;                 const size_t ro = (size_t)(u.row0 + ai * 128 + wr * 64 + m * 16 + fr) * DM + col0;
; #pragma unroll
;                 for (int bj = 0; bj < 2; ++bj) {
;                     const u32x4 gd = *(const u32x4*)(GDF + ro + bj * 32);
;                     const float ed[8] = {bf_lo(gd.x), bf_hi(gd.x), bf_lo(gd.y), bf_hi(gd.y), bf_lo(gd.z), bf_hi(gd.z), bf_lo(gd.w), bf_hi(gd.w)};
;                     if (u.tag == 0) {
;                         const u32x4 gn = *(const u32x4*)(GNA + ro + bj * 32);
;                         const float en[8] = {bf_lo(gn.x), bf_hi(gn.x), bf_lo(gn.y), bf_hi(gn.y), bf_lo(gn.z), bf_hi(gn.z), bf_lo(gn.w), bf_hi(gn.w)};
; #pragma unroll
;                         for (int e = 0; e < 8; ++e) {
;                             const float r = (1.0f + __builtin_amdgcn_exp2f(-1.4426950408889634f * ed[e])) * __builtin_amdgcn_rcpf(1.0f + __builtin_amdgcn_exp2f(-1.4426950408889634f * en[e]));
;                             acc[ai][bj][m][e >> 2][e & 3] *= r; }
;                     } else {
;                         float y[8];
; #pragma unroll
;                         for (int e = 0; e < 8; ++e) y[e] = acc[ai][bj][m][e >> 2][e & 3] * sigmoidf_fast(ed[e]) * (PSCALE * WSCALE_INV * OSCALE_INV);
;                         u32x2 w; w.x = pk4_fp8(y[0], y[1], y[2], y[3]); w.y = pk4_fp8(y[4], y[5], y[6], y[7]);
;                         *(LAS u32x2*)(my + fr * 80 + bj * 32 + fq * 8) = w;
;                     }
;                 }
.LBB0_585:
	s_nop 1
	v_add_u32_e32 v6, s76, v173
	v_ashrrev_i32_e32 v7, 31, v6
	v_lshlrev_b64 v[6:7], 11, v[6:7]
	v_lshl_add_u64 v[6:7], v[6:7], 0, v[2:3]
	v_lshl_add_u64 v[8:9], v[6:7], 1, s[40:41]
	global_load_dwordx4 v[156:159], v[8:9], off nt
	global_load_dwordx4 v[240:243], v[8:9], off offset:64 nt
	v_lshl_add_u64 v[252:253], v[6:7], 1, s[38:39]
	global_load_dwordx4 v[244:247], v[252:253], off nt
	global_load_dwordx4 v[248:251], v[252:253], off offset:64 nt
	s_and_b64 vcc, exec, s[4:5]
	s_mov_b64 s[58:59], -1
	s_waitcnt vmcnt(0)
	v_lshlrev_b32_e32 v5, 16, v156
	v_and_b32_e32 v156, 0xffff0000, v156
	v_lshlrev_b32_e32 v160, 16, v157
	v_and_b32_e32 v157, 0xffff0000, v157
	v_lshlrev_b32_e32 v161, 16, v158
	v_and_b32_e32 v158, 0xffff0000, v158
	v_lshlrev_b32_e32 v162, 16, v159
	v_and_b32_e32 v159, 0xffff0000, v159
	v_mul_f32_e32 v5, 0xbfb8aa3b, v5
	v_mul_f32_e32 v156, 0xbfb8aa3b, v156
	v_mul_f32_e32 v163, 0xbfb8aa3b, v160
	v_mul_f32_e32 v157, 0xbfb8aa3b, v157
	v_mul_f32_e32 v181, 0xbfb8aa3b, v161
	v_mul_f32_e32 v158, 0xbfb8aa3b, v158
	v_mul_f32_e32 v182, 0xbfb8aa3b, v162
	v_mul_f32_e32 v159, 0xbfb8aa3b, v159
	v_exp_f32_e32 v160, v5
	v_exp_f32_e32 v161, v156
	v_exp_f32_e32 v162, v163
	v_exp_f32_e32 v163, v157
	v_exp_f32_e32 v156, v181
	v_exp_f32_e32 v157, v158
	v_exp_f32_e32 v158, v182
	v_exp_f32_e32 v159, v159
	s_cbranch_vccnz .LBB0_587
	v_add_f32_e32 v182, 1.0, v162
	v_rcp_f32_e32 v182, v182
	v_add_f32_e32 v183, 1.0, v163
	v_rcp_f32_e32 v183, v183
	v_add_f32_e32 v184, 1.0, v156
	v_rcp_f32_e32 v184, v184
	v_mul_f32_e32 v182, v112, v182
	v_mul_f32_e32 v185, 0x3c000000, v182
	v_mul_f32_e32 v182, v113, v183
	v_add_f32_e32 v183, 1.0, v157
	v_mul_f32_e32 v186, 0x3c000000, v182
	v_mul_f32_e32 v182, v106, v184
	v_rcp_f32_e32 v183, v183
	v_add_f32_e32 v184, 1.0, v158
	v_rcp_f32_e32 v184, v184
	v_add_f32_e32 v5, 1.0, v160
	v_add_f32_e32 v181, 1.0, v161
	v_rcp_f32_e32 v5, v5
	v_rcp_f32_e32 v181, v181
	v_mul_f32_e32 v187, 0x3c000000, v182
	v_mul_f32_e32 v182, v107, v183
	v_mul_f32_e32 v188, 0x3c000000, v182
	v_mul_f32_e32 v182, v108, v184
	v_mul_f32_e32 v184, 0x3c000000, v182
	v_add_f32_e32 v182, 1.0, v159
	v_mul_f32_e32 v5, v110, v5
	v_mul_f32_e32 v181, v111, v181
	v_rcp_f32_e32 v189, v182
	v_mul_f32_e32 v5, 0x3c000000, v5
	v_mul_f32_e32 v181, 0x3c000000, v181
	v_mov_b32_e32 v182, 0
	v_mov_b32_e32 v183, 0
	v_cvt_pk_fp8_f32 v182, v5, v181
	v_cvt_pk_fp8_f32 v183, v187, v188
	v_mul_f32_e32 v5, v109, v189
	v_mul_f32_e32 v5, 0x3c000000, v5
	v_cvt_pk_fp8_f32 v182, v185, v186 op_sel:[0,0,1]
	v_cvt_pk_fp8_f32 v183, v184, v5 op_sel:[0,0,1]
	s_mov_b64 s[58:59], 0
	ds_write_b64 v180, v[182:183]

; #define LAS __attribute__((address_space(3)))
; __device__ __forceinline__ unsigned pk4_fp8(float a, float b, float c, float d) { int w = 0; w = __builtin_amdgcn_cvt_pk_fp8_f32(a, b, w, false); w = __builtin_amdgcn_cvt_pk_fp8_f32(c, d, w, true); return (unsigned)w; }
; __device__ __forceinline__ float bf_lo(unsigned w) { return __uint_as_float(w << 16); }
; __device__ __forceinline__ float bf_hi(unsigned w) { return __uint_as_float(w & 0xffff0000u); }
; __device__ __forceinline__ float sigmoidf_fast(float x) { return __builtin_amdgcn_rcpf(1.0f + __builtin_amdgcn_exp2f(-1.4426950408889634f * x)); }
;     __device__ __forceinline__ void operator()(f32x4 (&acc)[2][2][4][2], const Unit& u, int wr, int wc, int fr, int fq) const {
;     ...
;                 const size_t ro = (size_t)(u.row0 + ai * 128 + wr * 64 + m * 16 + fr) * DM + col0;
; #pragma unroll
;                 for (int bj = 0; bj < 2; ++bj) {
;                     const u32x4 gd = *(const u32x4*)(GDF + ro + bj * 32);
;                     const float ed[8] = {bf_lo(gd.x), bf_hi(gd.x), bf_lo(gd.y), bf_hi(gd.y), bf_lo(gd.z), bf_hi(gd.z), bf_lo(gd.w), bf_hi(gd.w)};
;                     if (u.tag == 0) {
;                         const u32x4 gn = *(const u32x4*)(GNA + ro + bj * 32);
;                         const float en[8] = {bf_lo(gn.x), bf_hi(gn.x), bf_lo(gn.y), bf_hi(gn.y), bf_lo(gn.z), bf_hi(gn.z), bf_lo(gn.w), bf_hi(gn.w)};
; #pragma unroll
;                         for (int e = 0; e < 8; ++e) {
;                             const float r = (1.0f + __builtin_amdgcn_exp2f(-1.4426950408889634f * ed[e])) * __builtin_amdgcn_rcpf(1.0f + __builtin_amdgcn_exp2f(-1.4426950408889634f * en[e]));
;                             acc[ai][bj][m][e >> 2][e & 3] *= r; }
;                     } else {
;                         float y[8];
; #pragma unroll
;                         for (int e = 0; e < 8; ++e) y[e] = acc[ai][bj][m][e >> 2][e & 3] * sigmoidf_fast(ed[e]) * (PSCALE * WSCALE_INV * OSCALE_INV);
;                         u32x2 w; w.x = pk4_fp8(y[0], y[1], y[2], y[3]); w.y = pk4_fp8(y[4], y[5], y[6], y[7]);
;                         *(LAS u32x2*)(my + fr * 80 + bj * 32 + fq * 8) = w;
;                     }
;                 }
.LBB0_593:
	s_nop 1
	v_add_u32_e32 v6, 0x80, v4
	v_ashrrev_i32_e32 v7, 31, v6
	v_lshlrev_b64 v[6:7], 11, v[6:7]
	v_lshl_add_u64 v[6:7], v[6:7], 0, v[2:3]
	v_lshl_add_u64 v[8:9], v[6:7], 1, s[40:41]
	global_load_dwordx4 v[156:159], v[8:9], off nt
	global_load_dwordx4 v[240:243], v[8:9], off offset:64 nt
	v_lshl_add_u64 v[252:253], v[6:7], 1, s[38:39]
	global_load_dwordx4 v[244:247], v[252:253], off nt
	global_load_dwordx4 v[248:251], v[252:253], off offset:64 nt
	s_and_b64 vcc, exec, s[4:5]
	s_mov_b64 s[58:59], -1
	s_waitcnt vmcnt(0)
	v_lshlrev_b32_e32 v5, 16, v156
	v_and_b32_e32 v156, 0xffff0000, v156
	v_lshlrev_b32_e32 v160, 16, v157
	v_and_b32_e32 v157, 0xffff0000, v157
	v_lshlrev_b32_e32 v161, 16, v158
	v_and_b32_e32 v158, 0xffff0000, v158
	v_lshlrev_b32_e32 v162, 16, v159
	v_and_b32_e32 v159, 0xffff0000, v159
	v_mul_f32_e32 v5, 0xbfb8aa3b, v5
	v_mul_f32_e32 v156, 0xbfb8aa3b, v156
	v_mul_f32_e32 v163, 0xbfb8aa3b, v160
	v_mul_f32_e32 v157, 0xbfb8aa3b, v157
	v_mul_f32_e32 v181, 0xbfb8aa3b, v161
	v_mul_f32_e32 v158, 0xbfb8aa3b, v158
	v_mul_f32_e32 v182, 0xbfb8aa3b, v162
	v_mul_f32_e32 v159, 0xbfb8aa3b, v159
	v_exp_f32_e32 v160, v5
	v_exp_f32_e32 v161, v156
	v_exp_f32_e32 v162, v163
	v_exp_f32_e32 v163, v157
	v_exp_f32_e32 v156, v181
	v_exp_f32_e32 v157, v158
	v_exp_f32_e32 v158, v182
	v_exp_f32_e32 v159, v159
	s_cbranch_vccnz .LBB0_595
	v_add_f32_e32 v182, 1.0, v162
	v_rcp_f32_e32 v182, v182
	v_add_f32_e32 v183, 1.0, v163
	v_rcp_f32_e32 v183, v183
	v_add_f32_e32 v184, 1.0, v156
	v_rcp_f32_e32 v184, v184
	v_mul_f32_e32 v182, v72, v182
	v_mul_f32_e32 v185, 0x3c000000, v182
	v_mul_f32_e32 v182, v73, v183
	v_add_f32_e32 v183, 1.0, v157
	v_mul_f32_e32 v186, 0x3c000000, v182
	v_mul_f32_e32 v182, v66, v184
	v_rcp_f32_e32 v183, v183
	v_add_f32_e32 v184, 1.0, v158
	v_rcp_f32_e32 v184, v184
	v_add_f32_e32 v5, 1.0, v160
	v_add_f32_e32 v181, 1.0, v161
	v_rcp_f32_e32 v5, v5
	v_rcp_f32_e32 v181, v181
	v_mul_f32_e32 v187, 0x3c000000, v182
	v_mul_f32_e32 v182, v67, v183
	v_mul_f32_e32 v188, 0x3c000000, v182
	v_mul_f32_e32 v182, v68, v184
	v_mul_f32_e32 v184, 0x3c000000, v182
	v_add_f32_e32 v182, 1.0, v159
	v_mul_f32_e32 v5, v70, v5
	v_mul_f32_e32 v181, v71, v181
	v_rcp_f32_e32 v189, v182
	v_mul_f32_e32 v5, 0x3c000000, v5
	v_mul_f32_e32 v181, 0x3c000000, v181
	v_mov_b32_e32 v182, 0
	v_mov_b32_e32 v183, 0
	v_cvt_pk_fp8_f32 v182, v5, v181
	v_cvt_pk_fp8_f32 v183, v187, v188
	v_mul_f32_e32 v5, v69, v189
	v_mul_f32_e32 v5, 0x3c000000, v5
	v_cvt_pk_fp8_f32 v182, v185, v186 op_sel:[0,0,1]
	v_cvt_pk_fp8_f32 v183, v184, v5 op_sel:[0,0,1]
	s_mov_b64 s[58:59], 0
	ds_write_b64 v180, v[182:183]

; #define LAS __attribute__((address_space(3)))
; __device__ __forceinline__ unsigned pk4_fp8(float a, float b, float c, float d) { int w = 0; w = __builtin_amdgcn_cvt_pk_fp8_f32(a, b, w, false); w = __builtin_amdgcn_cvt_pk_fp8_f32(c, d, w, true); return (unsigned)w; }
; __device__ __forceinline__ float bf_lo(unsigned w) { return __uint_as_float(w << 16); }
; __device__ __forceinline__ float bf_hi(unsigned w) { return __uint_as_float(w & 0xffff0000u); }
; __device__ __forceinline__ float sigmoidf_fast(float x) { return __builtin_amdgcn_rcpf(1.0f + __builtin_amdgcn_exp2f(-1.4426950408889634f * x)); }
;     __device__ __forceinline__ void operator()(f32x4 (&acc)[2][2][4][2], const Unit& u, int wr, int wc, int fr, int fq) const {
;     ...
;                 const size_t ro = (size_t)(u.row0 + ai * 128 + wr * 64 + m * 16 + fr) * DM + col0;
; #pragma unroll
;                 for (int bj = 0; bj < 2; ++bj) {
;                     const u32x4 gd = *(const u32x4*)(GDF + ro + bj * 32);
;                     const float ed[8] = {bf_lo(gd.x), bf_hi(gd.x), bf_lo(gd.y), bf_hi(gd.y), bf_lo(gd.z), bf_hi(gd.z), bf_lo(gd.w), bf_hi(gd.w)};
;                     if (u.tag == 0) {
;                         const u32x4 gn = *(const u32x4*)(GNA + ro + bj * 32);
;                         const float en[8] = {bf_lo(gn.x), bf_hi(gn.x), bf_lo(gn.y), bf_hi(gn.y), bf_lo(gn.z), bf_hi(gn.z), bf_lo(gn.w), bf_hi(gn.w)};
; #pragma unroll
;                         for (int e = 0; e < 8; ++e) {
;                             const float r = (1.0f + __builtin_amdgcn_exp2f(-1.4426950408889634f * ed[e])) * __builtin_amdgcn_rcpf(1.0f + __builtin_amdgcn_exp2f(-1.4426950408889634f * en[e]));
;                             acc[ai][bj][m][e >> 2][e & 3] *= r; }
;                     } else {
;                         float y[8];
; #pragma unroll
;                         for (int e = 0; e < 8; ++e) y[e] = acc[ai][bj][m][e >> 2][e & 3] * sigmoidf_fast(ed[e]) * (PSCALE * WSCALE_INV * OSCALE_INV);
;                         u32x2 w; w.x = pk4_fp8(y[0], y[1], y[2], y[3]); w.y = pk4_fp8(y[4], y[5], y[6], y[7]);
;                         *(LAS u32x2*)(my + fr * 80 + bj * 32 + fq * 8) = w;
;                     }
;                 }
.LBB0_601:
	s_nop 1
	v_add_u32_e32 v6, 0x90, v4
	v_ashrrev_i32_e32 v7, 31, v6
	v_lshlrev_b64 v[6:7], 11, v[6:7]
	v_lshl_add_u64 v[6:7], v[6:7], 0, v[2:3]
	v_lshl_add_u64 v[8:9], v[6:7], 1, s[40:41]
	global_load_dwordx4 v[156:159], v[8:9], off nt
	global_load_dwordx4 v[240:243], v[8:9], off offset:64 nt
	v_lshl_add_u64 v[252:253], v[6:7], 1, s[38:39]
	global_load_dwordx4 v[244:247], v[252:253], off nt
	global_load_dwordx4 v[248:251], v[252:253], off offset:64 nt
	s_and_b64 vcc, exec, s[4:5]
	s_mov_b64 s[58:59], -1
	s_waitcnt vmcnt(0)
	v_lshlrev_b32_e32 v5, 16, v156
	v_and_b32_e32 v156, 0xffff0000, v156
	v_lshlrev_b32_e32 v160, 16, v157
	v_and_b32_e32 v157, 0xffff0000, v157
	v_lshlrev_b32_e32 v161, 16, v158
	v_and_b32_e32 v158, 0xffff0000, v158
	v_lshlrev_b32_e32 v162, 16, v159
	v_and_b32_e32 v159, 0xffff0000, v159
	v_mul_f32_e32 v5, 0xbfb8aa3b, v5
	v_mul_f32_e32 v156, 0xbfb8aa3b, v156
	v_mul_f32_e32 v163, 0xbfb8aa3b, v160
	v_mul_f32_e32 v157, 0xbfb8aa3b, v157
	v_mul_f32_e32 v181, 0xbfb8aa3b, v161
	v_mul_f32_e32 v158, 0xbfb8aa3b, v158
	v_mul_f32_e32 v182, 0xbfb8aa3b, v162
	v_mul_f32_e32 v159, 0xbfb8aa3b, v159
	v_exp_f32_e32 v160, v5
	v_exp_f32_e32 v161, v156
	v_exp_f32_e32 v162, v163
	v_exp_f32_e32 v163, v157
	v_exp_f32_e32 v156, v181
	v_exp_f32_e32 v157, v158
	v_exp_f32_e32 v158, v182
	v_exp_f32_e32 v159, v159
	s_cbranch_vccnz .LBB0_603
	v_add_f32_e32 v182, 1.0, v162
	v_rcp_f32_e32 v182, v182
	v_add_f32_e32 v183, 1.0, v163
	v_rcp_f32_e32 v183, v183
	v_add_f32_e32 v184, 1.0, v156
	v_rcp_f32_e32 v184, v184
	v_mul_f32_e32 v182, v64, v182
	v_mul_f32_e32 v185, 0x3c000000, v182
	v_mul_f32_e32 v182, v65, v183
	v_add_f32_e32 v183, 1.0, v157
	v_mul_f32_e32 v186, 0x3c000000, v182
	v_mul_f32_e32 v182, v58, v184
	v_rcp_f32_e32 v183, v183
	v_add_f32_e32 v184, 1.0, v158
	v_rcp_f32_e32 v184, v184
	v_add_f32_e32 v5, 1.0, v160
	v_add_f32_e32 v181, 1.0, v161
	v_rcp_f32_e32 v5, v5
	v_rcp_f32_e32 v181, v181
	v_mul_f32_e32 v187, 0x3c000000, v182
	v_mul_f32_e32 v182, v59, v183
	v_mul_f32_e32 v188, 0x3c000000, v182
	v_mul_f32_e32 v182, v60, v184
	v_mul_f32_e32 v184, 0x3c000000, v182
	v_add_f32_e32 v182, 1.0, v159
	v_mul_f32_e32 v5, v62, v5
	v_mul_f32_e32 v181, v63, v181
	v_rcp_f32_e32 v189, v182
	v_mul_f32_e32 v5, 0x3c000000, v5
	v_mul_f32_e32 v181, 0x3c000000, v181
	v_mov_b32_e32 v182, 0
	v_mov_b32_e32 v183, 0
	v_cvt_pk_fp8_f32 v182, v5, v181
	v_cvt_pk_fp8_f32 v183, v187, v188
	v_mul_f32_e32 v5, v61, v189
	v_mul_f32_e32 v5, 0x3c000000, v5
	v_cvt_pk_fp8_f32 v182, v185, v186 op_sel:[0,0,1]
	v_cvt_pk_fp8_f32 v183, v184, v5 op_sel:[0,0,1]
	s_mov_b64 s[58:59], 0
	ds_write_b64 v180, v[182:183]

; #define LAS __attribute__((address_space(3)))
; __device__ __forceinline__ unsigned pk4_fp8(float a, float b, float c, float d) { int w = 0; w = __builtin_amdgcn_cvt_pk_fp8_f32(a, b, w, false); w = __builtin_amdgcn_cvt_pk_fp8_f32(c, d, w, true); return (unsigned)w; }
; __device__ __forceinline__ float bf_lo(unsigned w) { return __uint_as_float(w << 16); }
; __device__ __forceinline__ float bf_hi(unsigned w) { return __uint_as_float(w & 0xffff0000u); }
; __device__ __forceinline__ float sigmoidf_fast(float x) { return __builtin_amdgcn_rcpf(1.0f + __builtin_amdgcn_exp2f(-1.4426950408889634f * x)); }
;     __device__ __forceinline__ void operator()(f32x4 (&acc)[2][2][4][2], const Unit& u, int wr, int wc, int fr, int fq) const {
;     ...
;                 const size_t ro = (size_t)(u.row0 + ai * 128 + wr * 64 + m * 16 + fr) * DM + col0;
; #pragma unroll
;                 for (int bj = 0; bj < 2; ++bj) {
;                     const u32x4 gd = *(const u32x4*)(GDF + ro + bj * 32);
;                     const float ed[8] = {bf_lo(gd.x), bf_hi(gd.x), bf_lo(gd.y), bf_hi(gd.y), bf_lo(gd.z), bf_hi(gd.z), bf_lo(gd.w), bf_hi(gd.w)};
;                     if (u.tag == 0) {
;                         const u32x4 gn = *(const u32x4*)(GNA + ro + bj * 32);
;                         const float en[8] = {bf_lo(gn.x), bf_hi(gn.x), bf_lo(gn.y), bf_hi(gn.y), bf_lo(gn.z), bf_hi(gn.z), bf_lo(gn.w), bf_hi(gn.w)};
; #pragma unroll
;                         for (int e = 0; e < 8; ++e) {
;                             const float r = (1.0f + __builtin_amdgcn_exp2f(-1.4426950408889634f * ed[e])) * __builtin_amdgcn_rcpf(1.0f + __builtin_amdgcn_exp2f(-1.4426950408889634f * en[e]));
;                             acc[ai][bj][m][e >> 2][e & 3] *= r; }
;                     } else {
;                         float y[8];
; #pragma unroll
;                         for (int e = 0; e < 8; ++e) y[e] = acc[ai][bj][m][e >> 2][e & 3] * sigmoidf_fast(ed[e]) * (PSCALE * WSCALE_INV * OSCALE_INV);
;                         u32x2 w; w.x = pk4_fp8(y[0], y[1], y[2], y[3]); w.y = pk4_fp8(y[4], y[5], y[6], y[7]);
;                         *(LAS u32x2*)(my + fr * 80 + bj * 32 + fq * 8) = w;
;                     }
;                 }
.LBB0_609:
	s_nop 1
	v_add_u32_e32 v6, 0xa0, v4
	v_ashrrev_i32_e32 v7, 31, v6
	v_lshlrev_b64 v[6:7], 11, v[6:7]
	v_lshl_add_u64 v[6:7], v[6:7], 0, v[2:3]
	v_lshl_add_u64 v[8:9], v[6:7], 1, s[40:41]
	global_load_dwordx4 v[156:159], v[8:9], off nt
	global_load_dwordx4 v[240:243], v[8:9], off offset:64 nt
	v_lshl_add_u64 v[252:253], v[6:7], 1, s[38:39]
	global_load_dwordx4 v[244:247], v[252:253], off nt
	global_load_dwordx4 v[248:251], v[252:253], off offset:64 nt
	s_and_b64 vcc, exec, s[4:5]
	s_mov_b64 s[58:59], -1
	s_waitcnt vmcnt(0)
	v_lshlrev_b32_e32 v5, 16, v156
	v_and_b32_e32 v156, 0xffff0000, v156
	v_lshlrev_b32_e32 v160, 16, v157
	v_and_b32_e32 v157, 0xffff0000, v157
	v_lshlrev_b32_e32 v161, 16, v158
	v_and_b32_e32 v158, 0xffff0000, v158
	v_lshlrev_b32_e32 v162, 16, v159
	v_and_b32_e32 v159, 0xffff0000, v159
	v_mul_f32_e32 v5, 0xbfb8aa3b, v5
	v_mul_f32_e32 v156, 0xbfb8aa3b, v156
	v_mul_f32_e32 v163, 0xbfb8aa3b, v160
	v_mul_f32_e32 v157, 0xbfb8aa3b, v157
	v_mul_f32_e32 v181, 0xbfb8aa3b, v161
	v_mul_f32_e32 v158, 0xbfb8aa3b, v158
	v_mul_f32_e32 v182, 0xbfb8aa3b, v162
	v_mul_f32_e32 v159, 0xbfb8aa3b, v159
	v_exp_f32_e32 v160, v5
	v_exp_f32_e32 v161, v156
	v_exp_f32_e32 v162, v163
	v_exp_f32_e32 v163, v157
	v_exp_f32_e32 v156, v181
	v_exp_f32_e32 v157, v158
	v_exp_f32_e32 v158, v182
	v_exp_f32_e32 v159, v159
	s_cbranch_vccnz .LBB0_611
	v_add_f32_e32 v182, 1.0, v162
	v_rcp_f32_e32 v182, v182
	v_add_f32_e32 v183, 1.0, v163
	v_rcp_f32_e32 v183, v183
	v_add_f32_e32 v184, 1.0, v156
	v_rcp_f32_e32 v184, v184
	v_mul_f32_e32 v182, v56, v182
	v_mul_f32_e32 v185, 0x3c000000, v182
	v_mul_f32_e32 v182, v57, v183
	v_add_f32_e32 v183, 1.0, v157
	v_mul_f32_e32 v186, 0x3c000000, v182
	v_mul_f32_e32 v182, v50, v184
	v_rcp_f32_e32 v183, v183
	v_add_f32_e32 v184, 1.0, v158
	v_rcp_f32_e32 v184, v184
	v_add_f32_e32 v5, 1.0, v160
	v_add_f32_e32 v181, 1.0, v161
	v_rcp_f32_e32 v5, v5
	v_rcp_f32_e32 v181, v181
	v_mul_f32_e32 v187, 0x3c000000, v182
	v_mul_f32_e32 v182, v51, v183
	v_mul_f32_e32 v188, 0x3c000000, v182
	v_mul_f32_e32 v182, v52, v184
	v_mul_f32_e32 v184, 0x3c000000, v182
	v_add_f32_e32 v182, 1.0, v159
	v_mul_f32_e32 v5, v54, v5
	v_mul_f32_e32 v181, v55, v181
	v_rcp_f32_e32 v189, v182
	v_mul_f32_e32 v5, 0x3c000000, v5
	v_mul_f32_e32 v181, 0x3c000000, v181
	v_mov_b32_e32 v182, 0
	v_mov_b32_e32 v183, 0
	v_cvt_pk_fp8_f32 v182, v5, v181
	v_cvt_pk_fp8_f32 v183, v187, v188
	v_mul_f32_e32 v5, v53, v189
	v_mul_f32_e32 v5, 0x3c000000, v5
	v_cvt_pk_fp8_f32 v182, v185, v186 op_sel:[0,0,1]
	v_cvt_pk_fp8_f32 v183, v184, v5 op_sel:[0,0,1]
	s_mov_b64 s[58:59], 0
	ds_write_b64 v180, v[182:183]

; #define LAS __attribute__((address_space(3)))
; __device__ __forceinline__ unsigned pk4_fp8(float a, float b, float c, float d) { int w = 0; w = __builtin_amdgcn_cvt_pk_fp8_f32(a, b, w, false); w = __builtin_amdgcn_cvt_pk_fp8_f32(c, d, w, true); return (unsigned)w; }
; __device__ __forceinline__ float bf_lo(unsigned w) { return __uint_as_float(w << 16); }
; __device__ __forceinline__ float bf_hi(unsigned w) { return __uint_as_float(w & 0xffff0000u); }
; __device__ __forceinline__ float sigmoidf_fast(float x) { return __builtin_amdgcn_rcpf(1.0f + __builtin_amdgcn_exp2f(-1.4426950408889634f * x)); }
;     __device__ __forceinline__ void operator()(f32x4 (&acc)[2][2][4][2], const Unit& u, int wr, int wc, int fr, int fq) const {
;     ...
;                 const size_t ro = (size_t)(u.row0 + ai * 128 + wr * 64 + m * 16 + fr) * DM + col0;
; #pragma unroll
;                 for (int bj = 0; bj < 2; ++bj) {
;                     const u32x4 gd = *(const u32x4*)(GDF + ro + bj * 32);
;                     const float ed[8] = {bf_lo(gd.x), bf_hi(gd.x), bf_lo(gd.y), bf_hi(gd.y), bf_lo(gd.z), bf_hi(gd.z), bf_lo(gd.w), bf_hi(gd.w)};
;                     if (u.tag == 0) {
;                         const u32x4 gn = *(const u32x4*)(GNA + ro + bj * 32);
;                         const float en[8] = {bf_lo(gn.x), bf_hi(gn.x), bf_lo(gn.y), bf_hi(gn.y), bf_lo(gn.z), bf_hi(gn.z), bf_lo(gn.w), bf_hi(gn.w)};
; #pragma unroll
;                         for (int e = 0; e < 8; ++e) {
;                             const float r = (1.0f + __builtin_amdgcn_exp2f(-1.4426950408889634f * ed[e])) * __builtin_amdgcn_rcpf(1.0f + __builtin_amdgcn_exp2f(-1.4426950408889634f * en[e]));
;                             acc[ai][bj][m][e >> 2][e & 3] *= r; }
;                     } else {
;                         float y[8];
; #pragma unroll
;                         for (int e = 0; e < 8; ++e) y[e] = acc[ai][bj][m][e >> 2][e & 3] * sigmoidf_fast(ed[e]) * (PSCALE * WSCALE_INV * OSCALE_INV);
;                         u32x2 w; w.x = pk4_fp8(y[0], y[1], y[2], y[3]); w.y = pk4_fp8(y[4], y[5], y[6], y[7]);
;                         *(LAS u32x2*)(my + fr * 80 + bj * 32 + fq * 8) = w;
;                     }
;                 }
.LBB0_617:
	v_add_u32_e32 v4, 0xb0, v4
	v_ashrrev_i32_e32 v5, 31, v4
	v_lshlrev_b64 v[4:5], 11, v[4:5]
	v_lshl_add_u64 v[2:3], v[4:5], 0, v[2:3]
	v_lshl_add_u64 v[4:5], v[2:3], 1, s[40:41]
	global_load_dwordx4 v[6:9], v[4:5], off nt
	global_load_dwordx4 v[240:243], v[4:5], off offset:64 nt
	v_lshl_add_u64 v[252:253], v[2:3], 1, s[38:39]
	global_load_dwordx4 v[244:247], v[252:253], off nt
	global_load_dwordx4 v[248:251], v[252:253], off offset:64 nt
	s_and_b64 vcc, exec, s[4:5]
	s_mov_b64 s[58:59], -1
	s_waitcnt vmcnt(0)
	v_lshlrev_b32_e32 v156, 16, v6
	v_and_b32_e32 v6, 0xffff0000, v6
	v_lshlrev_b32_e32 v157, 16, v7
	v_and_b32_e32 v7, 0xffff0000, v7
	v_lshlrev_b32_e32 v158, 16, v8
	v_and_b32_e32 v8, 0xffff0000, v8
	v_lshlrev_b32_e32 v159, 16, v9
	v_and_b32_e32 v9, 0xffff0000, v9
	v_mul_f32_e32 v156, 0xbfb8aa3b, v156
	v_mul_f32_e32 v6, 0xbfb8aa3b, v6
	v_mul_f32_e32 v160, 0xbfb8aa3b, v157
	v_mul_f32_e32 v7, 0xbfb8aa3b, v7
	v_mul_f32_e32 v161, 0xbfb8aa3b, v158
	v_mul_f32_e32 v8, 0xbfb8aa3b, v8
	v_mul_f32_e32 v162, 0xbfb8aa3b, v159
	v_mul_f32_e32 v9, 0xbfb8aa3b, v9
	v_exp_f32_e32 v156, v156
	v_exp_f32_e32 v157, v6
	v_exp_f32_e32 v158, v160
	v_exp_f32_e32 v159, v7
	v_exp_f32_e32 v6, v161
	v_exp_f32_e32 v7, v8
	v_exp_f32_e32 v8, v162
	v_exp_f32_e32 v9, v9
	s_cbranch_vccnz .LBB0_619
	v_add_f32_e32 v160, 1.0, v156
	v_rcp_f32_e32 v160, v160
	v_add_f32_e32 v161, 1.0, v157
	v_add_f32_e32 v162, 1.0, v158
	v_rcp_f32_e32 v161, v161
	v_rcp_f32_e32 v162, v162
	v_mul_f32_e32 v160, v46, v160
	v_mul_f32_e32 v163, 0x3c000000, v160
	v_mul_f32_e32 v160, v47, v161
	v_mul_f32_e32 v161, 0x3c000000, v160
	v_mul_f32_e32 v160, v48, v162
	v_add_f32_e32 v162, 1.0, v159
	v_rcp_f32_e32 v162, v162
	v_add_f32_e32 v181, 1.0, v6
	v_rcp_f32_e32 v181, v181
	v_mul_f32_e32 v182, 0x3c000000, v160
	v_mul_f32_e32 v160, v49, v162
	v_mul_f32_e32 v162, 0x3c000000, v160
	v_mul_f32_e32 v160, v42, v181
	v_add_f32_e32 v181, 1.0, v7
	v_rcp_f32_e32 v181, v181
	v_add_f32_e32 v183, 1.0, v8
	v_rcp_f32_e32 v183, v183
	v_mul_f32_e32 v184, 0x3c000000, v160
	v_mul_f32_e32 v160, v43, v181
	v_mul_f32_e32 v181, 0x3c000000, v160
	v_mul_f32_e32 v160, v44, v183
	v_mul_f32_e32 v183, 0x3c000000, v160
	v_add_f32_e32 v160, 1.0, v9
	v_rcp_f32_e32 v185, v160
	v_mov_b32_e32 v160, 0
	v_cvt_pk_fp8_f32 v160, v163, v161
	v_mov_b32_e32 v161, 0
	v_cvt_pk_fp8_f32 v161, v184, v181
	v_mul_f32_e32 v163, v45, v185
	v_mul_f32_e32 v163, 0x3c000000, v163
	v_cvt_pk_fp8_f32 v160, v182, v162 op_sel:[0,0,1]
	v_cvt_pk_fp8_f32 v161, v183, v163 op_sel:[0,0,1]
	s_mov_b64 s[58:59], 0
	ds_write_b64 v180, v[160:161]

; __device__ __forceinline__ float bf_lo(unsigned w) { return __uint_as_float(w << 16); }
; __device__ __forceinline__ float bf_hi(unsigned w) { return __uint_as_float(w & 0xffff0000u); }
;     __device__ __forceinline__ void operator()(f32x4 (&acc)[2][2][4][2], const Unit& u, int wr, int wc, int fr, int fq) const {
;     ...
;                     if (u.tag == 0) {
;                         const u32x4 gn = *(const u32x4*)(GNA + ro + bj * 32);
;                         const float en[8] = {bf_lo(gn.x), bf_hi(gn.x), bf_lo(gn.y), bf_hi(gn.y), bf_lo(gn.z), bf_hi(gn.z), bf_lo(gn.w), bf_hi(gn.w)};
; #pragma unroll
;                         for (int e = 0; e < 8; ++e) {
;                             const float r = (1.0f + __builtin_amdgcn_exp2f(-1.4426950408889634f * ed[e])) * __builtin_amdgcn_rcpf(1.0f + __builtin_amdgcn_exp2f(-1.4426950408889634f * en[e]));
;                             acc[ai][bj][m][e >> 2][e & 3] *= r; }
.LBB0_625:
	v_mov_b64_e32 v[182:183], v[248:249]
	v_mov_b64_e32 v[184:185], v[250:251]
	v_pk_add_f32 v[8:9], v[160:161], 1.0 op_sel_hi:[1,0]
	v_pk_add_f32 v[158:159], v[158:159], 1.0 op_sel_hi:[1,0]
	v_pk_add_f32 v[156:157], v[156:157], 1.0 op_sel_hi:[1,0]
	v_pk_add_f32 v[6:7], v[6:7], 1.0 op_sel_hi:[1,0]
	s_waitcnt vmcnt(0)
	v_lshlrev_b32_e32 v5, 16, v182
	v_and_b32_e32 v160, 0xffff0000, v182
	v_lshlrev_b32_e32 v161, 16, v183
	v_and_b32_e32 v162, 0xffff0000, v183
	v_lshlrev_b32_e32 v163, 16, v184
	v_and_b32_e32 v181, 0xffff0000, v184
	v_lshlrev_b32_e32 v182, 16, v185
	v_and_b32_e32 v183, 0xffff0000, v185
	v_mul_f32_e32 v5, 0xbfb8aa3b, v5
	v_mul_f32_e32 v160, 0xbfb8aa3b, v160
	v_mul_f32_e32 v161, 0xbfb8aa3b, v161
	v_mul_f32_e32 v162, 0xbfb8aa3b, v162
	v_mul_f32_e32 v163, 0xbfb8aa3b, v163
	v_mul_f32_e32 v181, 0xbfb8aa3b, v181
	v_mul_f32_e32 v182, 0xbfb8aa3b, v182
	v_mul_f32_e32 v183, 0xbfb8aa3b, v183
	v_exp_f32_e32 v5, v5
	v_exp_f32_e32 v160, v160
	v_exp_f32_e32 v161, v161
	v_exp_f32_e32 v162, v162
	v_exp_f32_e32 v163, v163
	v_exp_f32_e32 v181, v181
	v_exp_f32_e32 v182, v182
	v_exp_f32_e32 v183, v183
	v_add_f32_e32 v5, 1.0, v5
	v_add_f32_e32 v184, 1.0, v160
	v_add_f32_e32 v185, 1.0, v161
	v_add_f32_e32 v186, 1.0, v162
	v_add_f32_e32 v187, 1.0, v163
	v_add_f32_e32 v181, 1.0, v181
	v_add_f32_e32 v188, 1.0, v182
	v_add_f32_e32 v189, 1.0, v183
	v_rcp_f32_e32 v160, v5
	v_rcp_f32_e32 v161, v184
	v_rcp_f32_e32 v162, v185
	v_rcp_f32_e32 v163, v186
	v_rcp_f32_e32 v182, v187
	v_rcp_f32_e32 v183, v181
	v_rcp_f32_e32 v184, v188
	v_rcp_f32_e32 v185, v189
	v_pk_mul_f32 v[158:159], v[158:159], v[160:161]
	v_pk_mul_f32 v[8:9], v[8:9], v[162:163]
	v_pk_mul_f32 v[6:7], v[6:7], v[182:183]
	v_pk_mul_f32 v[156:157], v[156:157], v[184:185]
	v_pk_mul_f32 v[104:105], v[104:105], v[8:9]
	v_pk_mul_f32 v[102:103], v[102:103], v[158:159]
	v_pk_mul_f32 v[100:101], v[100:101], v[156:157]
	v_pk_mul_f32 v[98:99], v[98:99], v[6:7]
	s_and_b64 vcc, exec, s[4:5]
	s_cbranch_vccz .LBB0_568
	s_branch .LBB0_569

; __device__ __forceinline__ float bf_lo(unsigned w) { return __uint_as_float(w << 16); }
; __device__ __forceinline__ float bf_hi(unsigned w) { return __uint_as_float(w & 0xffff0000u); }
;     __device__ __forceinline__ void operator()(f32x4 (&acc)[2][2][4][2], const Unit& u, int wr, int wc, int fr, int fq) const {
;     ...
;                     if (u.tag == 0) {
;                         const u32x4 gn = *(const u32x4*)(GNA + ro + bj * 32);
;                         const float en[8] = {bf_lo(gn.x), bf_hi(gn.x), bf_lo(gn.y), bf_hi(gn.y), bf_lo(gn.z), bf_hi(gn.z), bf_lo(gn.w), bf_hi(gn.w)};
; #pragma unroll
;                         for (int e = 0; e < 8; ++e) {
;                             const float r = (1.0f + __builtin_amdgcn_exp2f(-1.4426950408889634f * ed[e])) * __builtin_amdgcn_rcpf(1.0f + __builtin_amdgcn_exp2f(-1.4426950408889634f * en[e]));
;                             acc[ai][bj][m][e >> 2][e & 3] *= r; }
.LBB0_627:
	v_mov_b64_e32 v[182:183], v[248:249]
	v_mov_b64_e32 v[184:185], v[250:251]
	v_pk_add_f32 v[6:7], v[160:161], 1.0 op_sel_hi:[1,0]
	v_pk_add_f32 v[158:159], v[158:159], 1.0 op_sel_hi:[1,0]
	v_pk_add_f32 v[156:157], v[156:157], 1.0 op_sel_hi:[1,0]
	v_pk_add_f32 v[8:9], v[8:9], 1.0 op_sel_hi:[1,0]
	s_waitcnt vmcnt(0)
	v_lshlrev_b32_e32 v5, 16, v182
	v_and_b32_e32 v160, 0xffff0000, v182
	v_lshlrev_b32_e32 v161, 16, v183
	v_and_b32_e32 v162, 0xffff0000, v183
	v_lshlrev_b32_e32 v163, 16, v184
	v_and_b32_e32 v181, 0xffff0000, v184
	v_lshlrev_b32_e32 v182, 16, v185
	v_and_b32_e32 v183, 0xffff0000, v185
	v_mul_f32_e32 v5, 0xbfb8aa3b, v5
	v_mul_f32_e32 v160, 0xbfb8aa3b, v160
	v_mul_f32_e32 v161, 0xbfb8aa3b, v161
	v_mul_f32_e32 v162, 0xbfb8aa3b, v162
	v_mul_f32_e32 v163, 0xbfb8aa3b, v163
	v_mul_f32_e32 v181, 0xbfb8aa3b, v181
	v_mul_f32_e32 v182, 0xbfb8aa3b, v182
	v_mul_f32_e32 v183, 0xbfb8aa3b, v183
	v_exp_f32_e32 v5, v5
	v_exp_f32_e32 v160, v160
	v_exp_f32_e32 v161, v161
	v_exp_f32_e32 v162, v162
	v_exp_f32_e32 v163, v163
	v_exp_f32_e32 v181, v181
	v_exp_f32_e32 v182, v182
	v_exp_f32_e32 v183, v183
	v_add_f32_e32 v5, 1.0, v5
	v_add_f32_e32 v184, 1.0, v160
	v_add_f32_e32 v185, 1.0, v161
	v_add_f32_e32 v186, 1.0, v162
	v_add_f32_e32 v187, 1.0, v163
	v_add_f32_e32 v181, 1.0, v181
	v_add_f32_e32 v188, 1.0, v182
	v_add_f32_e32 v189, 1.0, v183
	v_rcp_f32_e32 v160, v5
	v_rcp_f32_e32 v161, v184
	v_rcp_f32_e32 v162, v185
	v_rcp_f32_e32 v163, v186
	v_rcp_f32_e32 v182, v187
	v_rcp_f32_e32 v183, v181
	v_rcp_f32_e32 v184, v188
	v_rcp_f32_e32 v185, v189
	v_pk_mul_f32 v[158:159], v[158:159], v[160:161]
	v_pk_mul_f32 v[6:7], v[6:7], v[162:163]
	v_pk_mul_f32 v[8:9], v[8:9], v[182:183]
	v_pk_mul_f32 v[156:157], v[156:157], v[184:185]
	v_pk_mul_f32 v[96:97], v[96:97], v[6:7]
	v_pk_mul_f32 v[94:95], v[94:95], v[158:159]
	v_pk_mul_f32 v[92:93], v[92:93], v[156:157]
	v_pk_mul_f32 v[90:91], v[90:91], v[8:9]
	s_and_b64 vcc, exec, s[4:5]
	s_cbranch_vccz .LBB0_576
	s_branch .LBB0_577

; __device__ __forceinline__ float bf_lo(unsigned w) { return __uint_as_float(w << 16); }
; __device__ __forceinline__ float bf_hi(unsigned w) { return __uint_as_float(w & 0xffff0000u); }
;     __device__ __forceinline__ void operator()(f32x4 (&acc)[2][2][4][2], const Unit& u, int wr, int wc, int fr, int fq) const {
;     ...
;                     if (u.tag == 0) {
;                         const u32x4 gn = *(const u32x4*)(GNA + ro + bj * 32);
;                         const float en[8] = {bf_lo(gn.x), bf_hi(gn.x), bf_lo(gn.y), bf_hi(gn.y), bf_lo(gn.z), bf_hi(gn.z), bf_lo(gn.w), bf_hi(gn.w)};
; #pragma unroll
;                         for (int e = 0; e < 8; ++e) {
;                             const float r = (1.0f + __builtin_amdgcn_exp2f(-1.4426950408889634f * ed[e])) * __builtin_amdgcn_rcpf(1.0f + __builtin_amdgcn_exp2f(-1.4426950408889634f * en[e]));
;                             acc[ai][bj][m][e >> 2][e & 3] *= r; }
.LBB0_629:
	v_mov_b64_e32 v[182:183], v[248:249]
	v_mov_b64_e32 v[184:185], v[250:251]
	v_pk_add_f32 v[6:7], v[160:161], 1.0 op_sel_hi:[1,0]
	v_pk_add_f32 v[158:159], v[158:159], 1.0 op_sel_hi:[1,0]
	v_pk_add_f32 v[156:157], v[156:157], 1.0 op_sel_hi:[1,0]
	v_pk_add_f32 v[8:9], v[8:9], 1.0 op_sel_hi:[1,0]
	s_waitcnt vmcnt(0)
	v_lshlrev_b32_e32 v5, 16, v182
	v_and_b32_e32 v160, 0xffff0000, v182
	v_lshlrev_b32_e32 v161, 16, v183
	v_and_b32_e32 v162, 0xffff0000, v183
	v_lshlrev_b32_e32 v163, 16, v184
	v_and_b32_e32 v181, 0xffff0000, v184
	v_lshlrev_b32_e32 v182, 16, v185
	v_and_b32_e32 v183, 0xffff0000, v185
	v_mul_f32_e32 v5, 0xbfb8aa3b, v5
	v_mul_f32_e32 v160, 0xbfb8aa3b, v160
	v_mul_f32_e32 v161, 0xbfb8aa3b, v161
	v_mul_f32_e32 v162, 0xbfb8aa3b, v162
	v_mul_f32_e32 v163, 0xbfb8aa3b, v163
	v_mul_f32_e32 v181, 0xbfb8aa3b, v181
	v_mul_f32_e32 v182, 0xbfb8aa3b, v182
	v_mul_f32_e32 v183, 0xbfb8aa3b, v183
	v_exp_f32_e32 v5, v5
	v_exp_f32_e32 v160, v160
	v_exp_f32_e32 v161, v161
	v_exp_f32_e32 v162, v162
	v_exp_f32_e32 v163, v163
	v_exp_f32_e32 v181, v181
	v_exp_f32_e32 v182, v182
	v_exp_f32_e32 v183, v183
	v_add_f32_e32 v5, 1.0, v5
	v_add_f32_e32 v184, 1.0, v160
	v_add_f32_e32 v185, 1.0, v161
	v_add_f32_e32 v186, 1.0, v162
	v_add_f32_e32 v187, 1.0, v163
	v_add_f32_e32 v181, 1.0, v181
	v_add_f32_e32 v188, 1.0, v182
	v_add_f32_e32 v189, 1.0, v183
	v_rcp_f32_e32 v160, v5
	v_rcp_f32_e32 v161, v184
	v_rcp_f32_e32 v162, v185
	v_rcp_f32_e32 v163, v186
	v_rcp_f32_e32 v182, v187
	v_rcp_f32_e32 v183, v181
	v_rcp_f32_e32 v184, v188
	v_rcp_f32_e32 v185, v189
	v_pk_mul_f32 v[158:159], v[158:159], v[160:161]
	v_pk_mul_f32 v[6:7], v[6:7], v[162:163]
	v_pk_mul_f32 v[8:9], v[8:9], v[182:183]
	v_pk_mul_f32 v[156:157], v[156:157], v[184:185]
	v_pk_mul_f32 v[88:89], v[88:89], v[6:7]
	v_pk_mul_f32 v[86:87], v[86:87], v[158:159]
	v_pk_mul_f32 v[84:85], v[84:85], v[156:157]
	v_pk_mul_f32 v[82:83], v[82:83], v[8:9]
	s_and_b64 vcc, exec, s[4:5]
	s_cbranch_vccz .LBB0_584
	s_branch .LBB0_585

; __device__ __forceinline__ float bf_lo(unsigned w) { return __uint_as_float(w << 16); }
; __device__ __forceinline__ float bf_hi(unsigned w) { return __uint_as_float(w & 0xffff0000u); }
;     __device__ __forceinline__ void operator()(f32x4 (&acc)[2][2][4][2], const Unit& u, int wr, int wc, int fr, int fq) const {
;     ...
;                     if (u.tag == 0) {
;                         const u32x4 gn = *(const u32x4*)(GNA + ro + bj * 32);
;                         const float en[8] = {bf_lo(gn.x), bf_hi(gn.x), bf_lo(gn.y), bf_hi(gn.y), bf_lo(gn.z), bf_hi(gn.z), bf_lo(gn.w), bf_hi(gn.w)};
; #pragma unroll
;                         for (int e = 0; e < 8; ++e) {
;                             const float r = (1.0f + __builtin_amdgcn_exp2f(-1.4426950408889634f * ed[e])) * __builtin_amdgcn_rcpf(1.0f + __builtin_amdgcn_exp2f(-1.4426950408889634f * en[e]));
;                             acc[ai][bj][m][e >> 2][e & 3] *= r; }
.LBB0_631:
	v_mov_b64_e32 v[182:183], v[248:249]
	v_mov_b64_e32 v[184:185], v[250:251]
	v_pk_add_f32 v[6:7], v[160:161], 1.0 op_sel_hi:[1,0]
	v_pk_add_f32 v[158:159], v[158:159], 1.0 op_sel_hi:[1,0]
	v_pk_add_f32 v[156:157], v[156:157], 1.0 op_sel_hi:[1,0]
	v_pk_add_f32 v[8:9], v[8:9], 1.0 op_sel_hi:[1,0]
	s_waitcnt vmcnt(0)
	v_lshlrev_b32_e32 v5, 16, v182
	v_and_b32_e32 v160, 0xffff0000, v182
	v_lshlrev_b32_e32 v161, 16, v183
	v_and_b32_e32 v162, 0xffff0000, v183
	v_lshlrev_b32_e32 v163, 16, v184
	v_and_b32_e32 v181, 0xffff0000, v184
	v_lshlrev_b32_e32 v182, 16, v185
	v_and_b32_e32 v183, 0xffff0000, v185
	v_mul_f32_e32 v5, 0xbfb8aa3b, v5
	v_mul_f32_e32 v160, 0xbfb8aa3b, v160
	v_mul_f32_e32 v161, 0xbfb8aa3b, v161
	v_mul_f32_e32 v162, 0xbfb8aa3b, v162
	v_mul_f32_e32 v163, 0xbfb8aa3b, v163
	v_mul_f32_e32 v181, 0xbfb8aa3b, v181
	v_mul_f32_e32 v182, 0xbfb8aa3b, v182
	v_mul_f32_e32 v183, 0xbfb8aa3b, v183
	v_exp_f32_e32 v5, v5
	v_exp_f32_e32 v160, v160
	v_exp_f32_e32 v161, v161
	v_exp_f32_e32 v162, v162
	v_exp_f32_e32 v163, v163
	v_exp_f32_e32 v181, v181
	v_exp_f32_e32 v182, v182
	v_exp_f32_e32 v183, v183
	v_add_f32_e32 v5, 1.0, v5
	v_add_f32_e32 v184, 1.0, v160
	v_add_f32_e32 v185, 1.0, v161
	v_add_f32_e32 v186, 1.0, v162
	v_add_f32_e32 v187, 1.0, v163
	v_add_f32_e32 v181, 1.0, v181
	v_add_f32_e32 v188, 1.0, v182
	v_add_f32_e32 v189, 1.0, v183
	v_rcp_f32_e32 v160, v5
	v_rcp_f32_e32 v161, v184
	v_rcp_f32_e32 v162, v185
	v_rcp_f32_e32 v163, v186
	v_rcp_f32_e32 v182, v187
	v_rcp_f32_e32 v183, v181
	v_rcp_f32_e32 v184, v188
	v_rcp_f32_e32 v185, v189
	v_pk_mul_f32 v[158:159], v[158:159], v[160:161]
	v_pk_mul_f32 v[6:7], v[6:7], v[162:163]
	v_pk_mul_f32 v[8:9], v[8:9], v[182:183]
	v_pk_mul_f32 v[156:157], v[156:157], v[184:185]
	v_pk_mul_f32 v[80:81], v[80:81], v[6:7]
	v_pk_mul_f32 v[78:79], v[78:79], v[158:159]
	v_pk_mul_f32 v[76:77], v[76:77], v[156:157]
	v_pk_mul_f32 v[74:75], v[74:75], v[8:9]
	s_and_b64 vcc, exec, s[4:5]
	s_cbranch_vccz .LBB0_592
	s_branch .LBB0_593

; __device__ __forceinline__ float bf_lo(unsigned w) { return __uint_as_float(w << 16); }
; __device__ __forceinline__ float bf_hi(unsigned w) { return __uint_as_float(w & 0xffff0000u); }
;     __device__ __forceinline__ void operator()(f32x4 (&acc)[2][2][4][2], const Unit& u, int wr, int wc, int fr, int fq) const {
;     ...
;                     if (u.tag == 0) {
;                         const u32x4 gn = *(const u32x4*)(GNA + ro + bj * 32);
;                         const float en[8] = {bf_lo(gn.x), bf_hi(gn.x), bf_lo(gn.y), bf_hi(gn.y), bf_lo(gn.z), bf_hi(gn.z), bf_lo(gn.w), bf_hi(gn.w)};
; #pragma unroll
;                         for (int e = 0; e < 8; ++e) {
;                             const float r = (1.0f + __builtin_amdgcn_exp2f(-1.4426950408889634f * ed[e])) * __builtin_amdgcn_rcpf(1.0f + __builtin_amdgcn_exp2f(-1.4426950408889634f * en[e]));
;                             acc[ai][bj][m][e >> 2][e & 3] *= r; }
.LBB0_633:
	v_mov_b64_e32 v[182:183], v[248:249]
	v_mov_b64_e32 v[184:185], v[250:251]
	v_pk_add_f32 v[6:7], v[160:161], 1.0 op_sel_hi:[1,0]
	v_pk_add_f32 v[158:159], v[158:159], 1.0 op_sel_hi:[1,0]
	v_pk_add_f32 v[156:157], v[156:157], 1.0 op_sel_hi:[1,0]
	v_pk_add_f32 v[8:9], v[8:9], 1.0 op_sel_hi:[1,0]
	s_waitcnt vmcnt(0)
	v_lshlrev_b32_e32 v5, 16, v182
	v_and_b32_e32 v160, 0xffff0000, v182
	v_lshlrev_b32_e32 v161, 16, v183
	v_and_b32_e32 v162, 0xffff0000, v183
	v_lshlrev_b32_e32 v163, 16, v184
	v_and_b32_e32 v181, 0xffff0000, v184
	v_lshlrev_b32_e32 v182, 16, v185
	v_and_b32_e32 v183, 0xffff0000, v185
	v_mul_f32_e32 v5, 0xbfb8aa3b, v5
	v_mul_f32_e32 v160, 0xbfb8aa3b, v160
	v_mul_f32_e32 v161, 0xbfb8aa3b, v161
	v_mul_f32_e32 v162, 0xbfb8aa3b, v162
	v_mul_f32_e32 v163, 0xbfb8aa3b, v163
	v_mul_f32_e32 v181, 0xbfb8aa3b, v181
	v_mul_f32_e32 v182, 0xbfb8aa3b, v182
	v_mul_f32_e32 v183, 0xbfb8aa3b, v183
	v_exp_f32_e32 v5, v5
	v_exp_f32_e32 v160, v160
	v_exp_f32_e32 v161, v161
	v_exp_f32_e32 v162, v162
	v_exp_f32_e32 v163, v163
	v_exp_f32_e32 v181, v181
	v_exp_f32_e32 v182, v182
	v_exp_f32_e32 v183, v183
	v_add_f32_e32 v5, 1.0, v5
	v_add_f32_e32 v184, 1.0, v160
	v_add_f32_e32 v185, 1.0, v161
	v_add_f32_e32 v186, 1.0, v162
	v_add_f32_e32 v187, 1.0, v163
	v_add_f32_e32 v181, 1.0, v181
	v_add_f32_e32 v188, 1.0, v182
	v_add_f32_e32 v189, 1.0, v183
	v_rcp_f32_e32 v160, v5
	v_rcp_f32_e32 v161, v184
	v_rcp_f32_e32 v162, v185
	v_rcp_f32_e32 v163, v186
	v_rcp_f32_e32 v182, v187
	v_rcp_f32_e32 v183, v181
	v_rcp_f32_e32 v184, v188
	v_rcp_f32_e32 v185, v189
	v_pk_mul_f32 v[158:159], v[158:159], v[160:161]
	v_pk_mul_f32 v[6:7], v[6:7], v[162:163]
	v_pk_mul_f32 v[8:9], v[8:9], v[182:183]
	v_pk_mul_f32 v[156:157], v[156:157], v[184:185]
	v_pk_mul_f32 v[40:41], v[40:41], v[6:7]
	v_pk_mul_f32 v[38:39], v[38:39], v[158:159]
	v_pk_mul_f32 v[36:37], v[36:37], v[156:157]
	v_pk_mul_f32 v[34:35], v[34:35], v[8:9]
	s_and_b64 vcc, exec, s[4:5]
	s_cbranch_vccz .LBB0_600
	s_branch .LBB0_601

; __device__ __forceinline__ float bf_lo(unsigned w) { return __uint_as_float(w << 16); }
; __device__ __forceinline__ float bf_hi(unsigned w) { return __uint_as_float(w & 0xffff0000u); }
;     __device__ __forceinline__ void operator()(f32x4 (&acc)[2][2][4][2], const Unit& u, int wr, int wc, int fr, int fq) const {
;     ...
;                     if (u.tag == 0) {
;                         const u32x4 gn = *(const u32x4*)(GNA + ro + bj * 32);
;                         const float en[8] = {bf_lo(gn.x), bf_hi(gn.x), bf_lo(gn.y), bf_hi(gn.y), bf_lo(gn.z), bf_hi(gn.z), bf_lo(gn.w), bf_hi(gn.w)};
; #pragma unroll
;                         for (int e = 0; e < 8; ++e) {
;                             const float r = (1.0f + __builtin_amdgcn_exp2f(-1.4426950408889634f * ed[e])) * __builtin_amdgcn_rcpf(1.0f + __builtin_amdgcn_exp2f(-1.4426950408889634f * en[e]));
;                             acc[ai][bj][m][e >> 2][e & 3] *= r; }
.LBB0_635:
	v_mov_b64_e32 v[182:183], v[248:249]
	v_mov_b64_e32 v[184:185], v[250:251]
	v_pk_add_f32 v[6:7], v[160:161], 1.0 op_sel_hi:[1,0]
	v_pk_add_f32 v[158:159], v[158:159], 1.0 op_sel_hi:[1,0]
	v_pk_add_f32 v[156:157], v[156:157], 1.0 op_sel_hi:[1,0]
	v_pk_add_f32 v[8:9], v[8:9], 1.0 op_sel_hi:[1,0]
	s_waitcnt vmcnt(0)
	v_lshlrev_b32_e32 v5, 16, v182
	v_and_b32_e32 v160, 0xffff0000, v182
	v_lshlrev_b32_e32 v161, 16, v183
	v_and_b32_e32 v162, 0xffff0000, v183
	v_lshlrev_b32_e32 v163, 16, v184
	v_and_b32_e32 v181, 0xffff0000, v184
	v_lshlrev_b32_e32 v182, 16, v185
	v_and_b32_e32 v183, 0xffff0000, v185
	v_mul_f32_e32 v5, 0xbfb8aa3b, v5
	v_mul_f32_e32 v160, 0xbfb8aa3b, v160
	v_mul_f32_e32 v161, 0xbfb8aa3b, v161
	v_mul_f32_e32 v162, 0xbfb8aa3b, v162
	v_mul_f32_e32 v163, 0xbfb8aa3b, v163
	v_mul_f32_e32 v181, 0xbfb8aa3b, v181
	v_mul_f32_e32 v182, 0xbfb8aa3b, v182
	v_mul_f32_e32 v183, 0xbfb8aa3b, v183
	v_exp_f32_e32 v5, v5
	v_exp_f32_e32 v160, v160
	v_exp_f32_e32 v161, v161
	v_exp_f32_e32 v162, v162
	v_exp_f32_e32 v163, v163
	v_exp_f32_e32 v181, v181
	v_exp_f32_e32 v182, v182
	v_exp_f32_e32 v183, v183
	v_add_f32_e32 v5, 1.0, v5
	v_add_f32_e32 v184, 1.0, v160
	v_add_f32_e32 v185, 1.0, v161
	v_add_f32_e32 v186, 1.0, v162
	v_add_f32_e32 v187, 1.0, v163
	v_add_f32_e32 v181, 1.0, v181
	v_add_f32_e32 v188, 1.0, v182
	v_add_f32_e32 v189, 1.0, v183
	v_rcp_f32_e32 v160, v5
	v_rcp_f32_e32 v161, v184
	v_rcp_f32_e32 v162, v185
	v_rcp_f32_e32 v163, v186
	v_rcp_f32_e32 v182, v187
	v_rcp_f32_e32 v183, v181
	v_rcp_f32_e32 v184, v188
	v_rcp_f32_e32 v185, v189
	v_pk_mul_f32 v[158:159], v[158:159], v[160:161]
	v_pk_mul_f32 v[6:7], v[6:7], v[162:163]
	v_pk_mul_f32 v[8:9], v[8:9], v[182:183]
	v_pk_mul_f32 v[156:157], v[156:157], v[184:185]
	v_pk_mul_f32 v[32:33], v[32:33], v[6:7]
	v_pk_mul_f32 v[30:31], v[30:31], v[158:159]
	v_pk_mul_f32 v[28:29], v[28:29], v[156:157]
	v_pk_mul_f32 v[26:27], v[26:27], v[8:9]
	s_and_b64 vcc, exec, s[4:5]
	s_cbranch_vccz .LBB0_608
	s_branch .LBB0_609

; __device__ __forceinline__ float bf_lo(unsigned w) { return __uint_as_float(w << 16); }
; __device__ __forceinline__ float bf_hi(unsigned w) { return __uint_as_float(w & 0xffff0000u); }
;     __device__ __forceinline__ void operator()(f32x4 (&acc)[2][2][4][2], const Unit& u, int wr, int wc, int fr, int fq) const {
;     ...
;                     if (u.tag == 0) {
;                         const u32x4 gn = *(const u32x4*)(GNA + ro + bj * 32);
;                         const float en[8] = {bf_lo(gn.x), bf_hi(gn.x), bf_lo(gn.y), bf_hi(gn.y), bf_lo(gn.z), bf_hi(gn.z), bf_lo(gn.w), bf_hi(gn.w)};
; #pragma unroll
;                         for (int e = 0; e < 8; ++e) {
;                             const float r = (1.0f + __builtin_amdgcn_exp2f(-1.4426950408889634f * ed[e])) * __builtin_amdgcn_rcpf(1.0f + __builtin_amdgcn_exp2f(-1.4426950408889634f * en[e]));
;                             acc[ai][bj][m][e >> 2][e & 3] *= r; }
.LBB0_637:
	v_mov_b64_e32 v[182:183], v[248:249]
	v_mov_b64_e32 v[184:185], v[250:251]
	v_pk_add_f32 v[6:7], v[160:161], 1.0 op_sel_hi:[1,0]
	v_pk_add_f32 v[158:159], v[158:159], 1.0 op_sel_hi:[1,0]
	v_pk_add_f32 v[156:157], v[156:157], 1.0 op_sel_hi:[1,0]
	v_pk_add_f32 v[8:9], v[8:9], 1.0 op_sel_hi:[1,0]
	s_waitcnt vmcnt(0)
	v_lshlrev_b32_e32 v5, 16, v182
	v_and_b32_e32 v160, 0xffff0000, v182
	v_lshlrev_b32_e32 v161, 16, v183
	v_and_b32_e32 v162, 0xffff0000, v183
	v_lshlrev_b32_e32 v163, 16, v184
	v_and_b32_e32 v181, 0xffff0000, v184
	v_lshlrev_b32_e32 v182, 16, v185
	v_and_b32_e32 v183, 0xffff0000, v185
	v_mul_f32_e32 v5, 0xbfb8aa3b, v5
	v_mul_f32_e32 v160, 0xbfb8aa3b, v160
	v_mul_f32_e32 v161, 0xbfb8aa3b, v161
	v_mul_f32_e32 v162, 0xbfb8aa3b, v162
	v_mul_f32_e32 v163, 0xbfb8aa3b, v163
	v_mul_f32_e32 v181, 0xbfb8aa3b, v181
	v_mul_f32_e32 v182, 0xbfb8aa3b, v182
	v_mul_f32_e32 v183, 0xbfb8aa3b, v183
	v_exp_f32_e32 v5, v5
	v_exp_f32_e32 v160, v160
	v_exp_f32_e32 v161, v161
	v_exp_f32_e32 v162, v162
	v_exp_f32_e32 v163, v163
	v_exp_f32_e32 v181, v181
	v_exp_f32_e32 v182, v182
	v_exp_f32_e32 v183, v183
	v_add_f32_e32 v5, 1.0, v5
	v_add_f32_e32 v184, 1.0, v160
	v_add_f32_e32 v185, 1.0, v161
	v_add_f32_e32 v186, 1.0, v162
	v_add_f32_e32 v187, 1.0, v163
	v_add_f32_e32 v181, 1.0, v181
	v_add_f32_e32 v188, 1.0, v182
	v_add_f32_e32 v189, 1.0, v183
	v_rcp_f32_e32 v160, v5
	v_rcp_f32_e32 v161, v184
	v_rcp_f32_e32 v162, v185
	v_rcp_f32_e32 v163, v186
	v_rcp_f32_e32 v182, v187
	v_rcp_f32_e32 v183, v181
	v_rcp_f32_e32 v184, v188
	v_rcp_f32_e32 v185, v189
	v_pk_mul_f32 v[158:159], v[158:159], v[160:161]
	v_pk_mul_f32 v[6:7], v[6:7], v[162:163]
	v_pk_mul_f32 v[8:9], v[8:9], v[182:183]
	v_pk_mul_f32 v[156:157], v[156:157], v[184:185]
	v_pk_mul_f32 v[24:25], v[24:25], v[6:7]
	v_pk_mul_f32 v[22:23], v[22:23], v[158:159]
	v_pk_mul_f32 v[20:21], v[20:21], v[156:157]
	v_pk_mul_f32 v[18:19], v[18:19], v[8:9]
	s_and_b64 vcc, exec, s[4:5]
	s_cbranch_vccz .LBB0_616
	s_branch .LBB0_617

; __device__ __forceinline__ float bf_lo(unsigned w) { return __uint_as_float(w << 16); }
; __device__ __forceinline__ float bf_hi(unsigned w) { return __uint_as_float(w & 0xffff0000u); }
;     __device__ __forceinline__ void operator()(f32x4 (&acc)[2][2][4][2], const Unit& u, int wr, int wc, int fr, int fq) const {
;     ...
;                     if (u.tag == 0) {
;                         const u32x4 gn = *(const u32x4*)(GNA + ro + bj * 32);
;                         const float en[8] = {bf_lo(gn.x), bf_hi(gn.x), bf_lo(gn.y), bf_hi(gn.y), bf_lo(gn.z), bf_hi(gn.z), bf_lo(gn.w), bf_hi(gn.w)};
; #pragma unroll
;                         for (int e = 0; e < 8; ++e) {
;                             const float r = (1.0f + __builtin_amdgcn_exp2f(-1.4426950408889634f * ed[e])) * __builtin_amdgcn_rcpf(1.0f + __builtin_amdgcn_exp2f(-1.4426950408889634f * en[e]));
;                             acc[ai][bj][m][e >> 2][e & 3] *= r; }
.LBB0_639:
	v_mov_b64_e32 v[158:159], v[248:249]
	v_mov_b64_e32 v[160:161], v[250:251]
	v_pk_add_f32 v[2:3], v[156:157], 1.0 op_sel_hi:[1,0]
	v_pk_add_f32 v[8:9], v[8:9], 1.0 op_sel_hi:[1,0]
	v_pk_add_f32 v[6:7], v[6:7], 1.0 op_sel_hi:[1,0]
	v_pk_add_f32 v[4:5], v[4:5], 1.0 op_sel_hi:[1,0]
	s_waitcnt vmcnt(0)
	v_lshlrev_b32_e32 v156, 16, v158
	v_and_b32_e32 v157, 0xffff0000, v158
	v_lshlrev_b32_e32 v158, 16, v159
	v_and_b32_e32 v159, 0xffff0000, v159
	v_lshlrev_b32_e32 v162, 16, v160
	v_and_b32_e32 v160, 0xffff0000, v160
	v_lshlrev_b32_e32 v163, 16, v161
	v_and_b32_e32 v161, 0xffff0000, v161
	v_mul_f32_e32 v156, 0xbfb8aa3b, v156
	v_mul_f32_e32 v157, 0xbfb8aa3b, v157
	v_mul_f32_e32 v158, 0xbfb8aa3b, v158
	v_mul_f32_e32 v159, 0xbfb8aa3b, v159
	v_mul_f32_e32 v162, 0xbfb8aa3b, v162
	v_mul_f32_e32 v160, 0xbfb8aa3b, v160
	v_mul_f32_e32 v163, 0xbfb8aa3b, v163
	v_mul_f32_e32 v161, 0xbfb8aa3b, v161
	v_exp_f32_e32 v156, v156
	v_exp_f32_e32 v157, v157
	v_exp_f32_e32 v158, v158
	v_exp_f32_e32 v159, v159
	v_exp_f32_e32 v162, v162
	v_exp_f32_e32 v160, v160
	v_exp_f32_e32 v163, v163
	v_exp_f32_e32 v161, v161
	v_add_f32_e32 v156, 1.0, v156
	v_add_f32_e32 v157, 1.0, v157
	v_add_f32_e32 v158, 1.0, v158
	v_add_f32_e32 v159, 1.0, v159
	v_add_f32_e32 v162, 1.0, v162
	v_add_f32_e32 v181, 1.0, v160
	v_add_f32_e32 v163, 1.0, v163
	v_add_f32_e32 v182, 1.0, v161
	v_rcp_f32_e32 v156, v156
	v_rcp_f32_e32 v157, v157
	v_rcp_f32_e32 v158, v158
	v_rcp_f32_e32 v159, v159
	v_rcp_f32_e32 v160, v162
	v_rcp_f32_e32 v161, v181
	v_rcp_f32_e32 v162, v163
	v_rcp_f32_e32 v163, v182
	v_pk_mul_f32 v[8:9], v[8:9], v[156:157]
	v_pk_mul_f32 v[2:3], v[2:3], v[158:159]
	v_pk_mul_f32 v[4:5], v[4:5], v[160:161]
	v_pk_mul_f32 v[6:7], v[6:7], v[162:163]
	v_pk_mul_f32 v[16:17], v[16:17], v[2:3]
	v_pk_mul_f32 v[14:15], v[14:15], v[8:9]
	v_pk_mul_f32 v[12:13], v[12:13], v[6:7]
	v_pk_mul_f32 v[10:11], v[10:11], v[4:5]
	s_mov_b64 s[4:5], -1
	s_and_b64 vcc, exec, s[50:51]
	s_cbranch_vccz .LBB0_554
